# write-through (sc0 sc1) on the full-line fp8 H2 row stores of phase 6, to shorten the L2 write-back at the following grid barrier
# speedup vs baseline: 1.0055x; 1.0055x over previous
; __device__ __forceinline__ void phase_router(const Args& a, unsigned char* lds_g, int tid, int lane, int wave) {
;     ...
;         __syncthreads();
; #pragma unroll
;         for (int r = 0; r < 4; ++r) { const int tl = 4 * kq + r, t = tok0 + tl; const float rstd = RS[slot * 16 + tl];
;             const unsigned long long* xrow = (const unsigned long long*)(X1 + (size_t)t * D) + lane; unsigned* o4 = (unsigned*)((unsigned char*)H2 + (size_t)t * D) + lane;
;             f32x4 yv[8];
; #pragma unroll
;             for (int j = 0; j < 8; ++j) { const int c = 4 * lane + 256 * j;
;                 f32x4 gs, sh; if (shp) { gs = PSH[lane + 64 * j]; sh = PSH[512 + lane + 64 * j]; } else { const f32x4 gg = *(const f32x4*)(g + c), sc = *(const f32x4*)(MOD + b * 12288 + 4 * 2048 + c); gs = gg * (sc + 1.f); sh = *(const f32x4*)(MOD + b * 12288 + 3 * 2048 + c); }
;                 const unsigned long long xw = xrow[64 * j]; const f32x4 xv4 = (f32x4){bflo((unsigned)xw), bfhi((unsigned)xw), bflo((unsigned)(xw >> 32)), bfhi((unsigned)(xw >> 32))};
;                 yv[j] = xv4 * rstd * gs + sh; }
; #pragma unroll
;             for (int j = 0; j < 8; ++j) { int w8 = __builtin_amdgcn_cvt_pk_fp8_f32(yv[j].x, yv[j].y, 0, false); w8 = __builtin_amdgcn_cvt_pk_fp8_f32(yv[j].z, yv[j].w, w8, true); o4[64 * j] = (unsigned)w8; } }
.LBB0_985:
	s_mul_i32 s4, s30, 0x3000
	s_ashr_i32 s5, s4, 31
	s_lshl_b64 s[4:5], s[4:5], 2
	s_add_u32 s4, s2, s4
	s_addc_u32 s5, s3, s5
	v_mov_b32_e32 v0, s40
	s_waitcnt lgkmcnt(0)
	s_barrier
	s_and_b64 vcc, exec, s[18:19]
	s_cbranch_vccnz .Lh2_old
	s_or_b32 s28, s56, s37
	s_lshl_b32 s4, s28, 12
	s_mov_b32 s5, 0
	v_lshl_add_u64 v[210:211], v[66:67], 0, s[4:5]
	global_load_dwordx2 v[114:115], v[210:211], off
	global_load_dwordx2 v[116:117], v[210:211], off offset:512
	global_load_dwordx2 v[118:119], v[210:211], off offset:1024
	global_load_dwordx2 v[120:121], v[210:211], off offset:1536
	global_load_dwordx2 v[122:123], v[210:211], off offset:2048
	global_load_dwordx2 v[124:125], v[210:211], off offset:2560
	global_load_dwordx2 v[126:127], v[210:211], off offset:3072
	global_load_dwordx2 v[128:129], v[210:211], off offset:3584
	s_add_u32 s4, s4, 0x1000
	v_lshl_add_u64 v[210:211], v[66:67], 0, s[4:5]
	global_load_dwordx2 v[130:131], v[210:211], off
	global_load_dwordx2 v[132:133], v[210:211], off offset:512
	global_load_dwordx2 v[134:135], v[210:211], off offset:1024
	global_load_dwordx2 v[136:137], v[210:211], off offset:1536
	global_load_dwordx2 v[138:139], v[210:211], off offset:2048
	global_load_dwordx2 v[140:141], v[210:211], off offset:2560
	global_load_dwordx2 v[142:143], v[210:211], off offset:3072
	global_load_dwordx2 v[144:145], v[210:211], off offset:3584
	s_add_u32 s4, s4, 0x1000
	v_lshl_add_u64 v[210:211], v[66:67], 0, s[4:5]
	global_load_dwordx2 v[146:147], v[210:211], off
	global_load_dwordx2 v[148:149], v[210:211], off offset:512
	global_load_dwordx2 v[150:151], v[210:211], off offset:1024
	global_load_dwordx2 v[152:153], v[210:211], off offset:1536
	global_load_dwordx2 v[154:155], v[210:211], off offset:2048
	global_load_dwordx2 v[156:157], v[210:211], off offset:2560
	global_load_dwordx2 v[158:159], v[210:211], off offset:3072
	global_load_dwordx2 v[160:161], v[210:211], off offset:3584
	s_add_u32 s4, s4, 0x1000
	v_lshl_add_u64 v[210:211], v[66:67], 0, s[4:5]
	global_load_dwordx2 v[162:163], v[210:211], off
	global_load_dwordx2 v[164:165], v[210:211], off offset:512
	global_load_dwordx2 v[166:167], v[210:211], off offset:1024
	global_load_dwordx2 v[168:169], v[210:211], off offset:1536
	global_load_dwordx2 v[170:171], v[210:211], off offset:2048
	global_load_dwordx2 v[172:173], v[210:211], off offset:2560
	global_load_dwordx2 v[194:195], v[210:211], off offset:3072
	global_load_dwordx2 v[196:197], v[210:211], off offset:3584
	v_mov_b32_e32 v212, s40
	ds_read_b32 v202, v212 offset:50176
	ds_read_b32 v204, v212 offset:50180
	ds_read_b32 v206, v212 offset:50184
	ds_read_b32 v208, v212 offset:50188
	ds_read_b128 v[0:3], v183
	ds_read_b128 v[4:7], v183 offset:1024
	ds_read_b128 v[8:11], v183 offset:2048
	ds_read_b128 v[12:15], v183 offset:3072
	ds_read_b128 v[16:19], v183 offset:4096
	ds_read_b128 v[20:23], v183 offset:5120
	ds_read_b128 v[24:27], v183 offset:6144
	ds_read_b128 v[28:31], v183 offset:7168
	ds_read_b128 v[32:35], v183 offset:8192
	ds_read_b128 v[36:39], v183 offset:9216
	ds_read_b128 v[40:43], v183 offset:10240
	ds_read_b128 v[44:47], v183 offset:11264
	ds_read_b128 v[48:51], v183 offset:12288
	ds_read_b128 v[52:55], v183 offset:13312
	ds_read_b128 v[56:59], v183 offset:14336
	ds_read_b128 v[198:201], v183 offset:15360
	s_lshl_b32 s4, s28, 11
	s_waitcnt lgkmcnt(0)
	v_lshl_add_u64 v[210:211], v[68:69], 0, s[4:5]
	s_waitcnt vmcnt(24)
	v_lshlrev_b32_e32 v212, 16, v114
	v_and_b32_e32 v213, 0xffff0000, v114
	v_pk_mul_f32 v[212:213], v[202:203], v[212:213] op_sel_hi:[0,1]
	v_lshlrev_b32_e32 v114, 16, v115
	v_and_b32_e32 v115, 0xffff0000, v115
	v_pk_mul_f32 v[114:115], v[202:203], v[114:115] op_sel_hi:[0,1]
	v_pk_fma_f32 v[212:213], v[0:1], v[212:213], v[32:33]
	v_pk_fma_f32 v[114:115], v[2:3], v[114:115], v[34:35]
	v_cvt_pk_fp8_f32 v214, v212, v213
	v_cvt_pk_fp8_f32 v214, v114, v115 op_sel:[0,0,1]
	global_store_dword v[210:211], v214, off sc0 sc1
	v_lshlrev_b32_e32 v212, 16, v116
	v_and_b32_e32 v213, 0xffff0000, v116
	v_pk_mul_f32 v[212:213], v[202:203], v[212:213] op_sel_hi:[0,1]
	v_lshlrev_b32_e32 v116, 16, v117
	v_and_b32_e32 v117, 0xffff0000, v117
	v_pk_mul_f32 v[116:117], v[202:203], v[116:117] op_sel_hi:[0,1]
	v_pk_fma_f32 v[212:213], v[4:5], v[212:213], v[36:37]
	v_pk_fma_f32 v[116:117], v[6:7], v[116:117], v[38:39]
	v_cvt_pk_fp8_f32 v215, v212, v213
	v_cvt_pk_fp8_f32 v215, v116, v117 op_sel:[0,0,1]
	global_store_dword v[210:211], v215, off offset:256 sc0 sc1
	v_lshlrev_b32_e32 v212, 16, v118
	v_and_b32_e32 v213, 0xffff0000, v118
	v_pk_mul_f32 v[212:213], v[202:203], v[212:213] op_sel_hi:[0,1]
	v_lshlrev_b32_e32 v118, 16, v119
	v_and_b32_e32 v119, 0xffff0000, v119
	v_pk_mul_f32 v[118:119], v[202:203], v[118:119] op_sel_hi:[0,1]
	v_pk_fma_f32 v[212:213], v[8:9], v[212:213], v[40:41]
	v_pk_fma_f32 v[118:119], v[10:11], v[118:119], v[42:43]
	v_cvt_pk_fp8_f32 v214, v212, v213
	v_cvt_pk_fp8_f32 v214, v118, v119 op_sel:[0,0,1]
	global_store_dword v[210:211], v214, off offset:512 sc0 sc1
	v_lshlrev_b32_e32 v212, 16, v120
	v_and_b32_e32 v213, 0xffff0000, v120
	v_pk_mul_f32 v[212:213], v[202:203], v[212:213] op_sel_hi:[0,1]
	v_lshlrev_b32_e32 v120, 16, v121
	v_and_b32_e32 v121, 0xffff0000, v121
	v_pk_mul_f32 v[120:121], v[202:203], v[120:121] op_sel_hi:[0,1]
	v_pk_fma_f32 v[212:213], v[12:13], v[212:213], v[44:45]
	v_pk_fma_f32 v[120:121], v[14:15], v[120:121], v[46:47]
	v_cvt_pk_fp8_f32 v215, v212, v213
	v_cvt_pk_fp8_f32 v215, v120, v121 op_sel:[0,0,1]
	global_store_dword v[210:211], v215, off offset:768 sc0 sc1
	v_lshlrev_b32_e32 v212, 16, v122
	v_and_b32_e32 v213, 0xffff0000, v122
	v_pk_mul_f32 v[212:213], v[202:203], v[212:213] op_sel_hi:[0,1]
; __device__ __forceinline__ void phase_router(const Args& a, unsigned char* lds_g, int tid, int lane, int wave) {
;     ...
;         for (int r = 0; r < 4; ++r) { const int tl = 4 * kq + r, t = tok0 + tl; const float rstd = RS[slot * 16 + tl];
;             const unsigned long long* xrow = (const unsigned long long*)(X1 + (size_t)t * D) + lane; unsigned* o4 = (unsigned*)((unsigned char*)H2 + (size_t)t * D) + lane;
;             f32x4 yv[8];
; #pragma unroll
;             for (int j = 0; j < 8; ++j) { const int c = 4 * lane + 256 * j;
;                 f32x4 gs, sh; if (shp) { gs = PSH[lane + 64 * j]; sh = PSH[512 + lane + 64 * j]; } else { const f32x4 gg = *(const f32x4*)(g + c), sc = *(const f32x4*)(MOD + b * 12288 + 4 * 2048 + c); gs = gg * (sc + 1.f); sh = *(const f32x4*)(MOD + b * 12288 + 3 * 2048 + c); }
;                 const unsigned long long xw = xrow[64 * j]; const f32x4 xv4 = (f32x4){bflo((unsigned)xw), bfhi((unsigned)xw), bflo((unsigned)(xw >> 32)), bfhi((unsigned)(xw >> 32))};
;                 yv[j] = xv4 * rstd * gs + sh; }
; #pragma unroll
;             for (int j = 0; j < 8; ++j) { int w8 = __builtin_amdgcn_cvt_pk_fp8_f32(yv[j].x, yv[j].y, 0, false); w8 = __builtin_amdgcn_cvt_pk_fp8_f32(yv[j].z, yv[j].w, w8, true); o4[64 * j] = (unsigned)w8; } }
	v_lshlrev_b32_e32 v122, 16, v123
	v_and_b32_e32 v123, 0xffff0000, v123
	v_pk_mul_f32 v[122:123], v[202:203], v[122:123] op_sel_hi:[0,1]
	v_pk_fma_f32 v[212:213], v[16:17], v[212:213], v[48:49]
	v_pk_fma_f32 v[122:123], v[18:19], v[122:123], v[50:51]
	v_cvt_pk_fp8_f32 v214, v212, v213
	v_cvt_pk_fp8_f32 v214, v122, v123 op_sel:[0,0,1]
	global_store_dword v[210:211], v214, off offset:1024 sc0 sc1
	v_lshlrev_b32_e32 v212, 16, v124
	v_and_b32_e32 v213, 0xffff0000, v124
	v_pk_mul_f32 v[212:213], v[202:203], v[212:213] op_sel_hi:[0,1]
	v_lshlrev_b32_e32 v124, 16, v125
	v_and_b32_e32 v125, 0xffff0000, v125
	v_pk_mul_f32 v[124:125], v[202:203], v[124:125] op_sel_hi:[0,1]
	v_pk_fma_f32 v[212:213], v[20:21], v[212:213], v[52:53]
	v_pk_fma_f32 v[124:125], v[22:23], v[124:125], v[54:55]
	v_cvt_pk_fp8_f32 v215, v212, v213
	v_cvt_pk_fp8_f32 v215, v124, v125 op_sel:[0,0,1]
	global_store_dword v[210:211], v215, off offset:1280 sc0 sc1
	v_lshlrev_b32_e32 v212, 16, v126
	v_and_b32_e32 v213, 0xffff0000, v126
	v_pk_mul_f32 v[212:213], v[202:203], v[212:213] op_sel_hi:[0,1]
	v_lshlrev_b32_e32 v126, 16, v127
	v_and_b32_e32 v127, 0xffff0000, v127
	v_pk_mul_f32 v[126:127], v[202:203], v[126:127] op_sel_hi:[0,1]
	v_pk_fma_f32 v[212:213], v[24:25], v[212:213], v[56:57]
	v_pk_fma_f32 v[126:127], v[26:27], v[126:127], v[58:59]
	v_cvt_pk_fp8_f32 v214, v212, v213
	v_cvt_pk_fp8_f32 v214, v126, v127 op_sel:[0,0,1]
	global_store_dword v[210:211], v214, off offset:1536 sc0 sc1
	v_lshlrev_b32_e32 v212, 16, v128
	v_and_b32_e32 v213, 0xffff0000, v128
	v_pk_mul_f32 v[212:213], v[202:203], v[212:213] op_sel_hi:[0,1]
	v_lshlrev_b32_e32 v128, 16, v129
	v_and_b32_e32 v129, 0xffff0000, v129
	v_pk_mul_f32 v[128:129], v[202:203], v[128:129] op_sel_hi:[0,1]
	v_pk_fma_f32 v[212:213], v[28:29], v[212:213], v[198:199]
	v_pk_fma_f32 v[128:129], v[30:31], v[128:129], v[200:201]
	v_cvt_pk_fp8_f32 v215, v212, v213
	v_cvt_pk_fp8_f32 v215, v128, v129 op_sel:[0,0,1]
	global_store_dword v[210:211], v215, off offset:1792 sc0 sc1
	s_add_u32 s4, s4, 0x800
	v_lshl_add_u64 v[210:211], v[68:69], 0, s[4:5]
	s_waitcnt vmcnt(24)
	v_lshlrev_b32_e32 v212, 16, v130
	v_and_b32_e32 v213, 0xffff0000, v130
	v_pk_mul_f32 v[212:213], v[204:205], v[212:213] op_sel_hi:[0,1]
	v_lshlrev_b32_e32 v130, 16, v131
	v_and_b32_e32 v131, 0xffff0000, v131
	v_pk_mul_f32 v[130:131], v[204:205], v[130:131] op_sel_hi:[0,1]
	v_pk_fma_f32 v[212:213], v[0:1], v[212:213], v[32:33]
	v_pk_fma_f32 v[130:131], v[2:3], v[130:131], v[34:35]
	v_cvt_pk_fp8_f32 v214, v212, v213
	v_cvt_pk_fp8_f32 v214, v130, v131 op_sel:[0,0,1]
	global_store_dword v[210:211], v214, off sc0 sc1
	v_lshlrev_b32_e32 v212, 16, v132
	v_and_b32_e32 v213, 0xffff0000, v132
	v_pk_mul_f32 v[212:213], v[204:205], v[212:213] op_sel_hi:[0,1]
	v_lshlrev_b32_e32 v132, 16, v133
	v_and_b32_e32 v133, 0xffff0000, v133
	v_pk_mul_f32 v[132:133], v[204:205], v[132:133] op_sel_hi:[0,1]
	v_pk_fma_f32 v[212:213], v[4:5], v[212:213], v[36:37]
	v_pk_fma_f32 v[132:133], v[6:7], v[132:133], v[38:39]
	v_cvt_pk_fp8_f32 v215, v212, v213
	v_cvt_pk_fp8_f32 v215, v132, v133 op_sel:[0,0,1]
	global_store_dword v[210:211], v215, off offset:256 sc0 sc1
	v_lshlrev_b32_e32 v212, 16, v134
	v_and_b32_e32 v213, 0xffff0000, v134
	v_pk_mul_f32 v[212:213], v[204:205], v[212:213] op_sel_hi:[0,1]
	v_lshlrev_b32_e32 v134, 16, v135
	v_and_b32_e32 v135, 0xffff0000, v135
	v_pk_mul_f32 v[134:135], v[204:205], v[134:135] op_sel_hi:[0,1]
	v_pk_fma_f32 v[212:213], v[8:9], v[212:213], v[40:41]
	v_pk_fma_f32 v[134:135], v[10:11], v[134:135], v[42:43]
	v_cvt_pk_fp8_f32 v214, v212, v213
	v_cvt_pk_fp8_f32 v214, v134, v135 op_sel:[0,0,1]
	global_store_dword v[210:211], v214, off offset:512 sc0 sc1
	v_lshlrev_b32_e32 v212, 16, v136
	v_and_b32_e32 v213, 0xffff0000, v136
	v_pk_mul_f32 v[212:213], v[204:205], v[212:213] op_sel_hi:[0,1]
	v_lshlrev_b32_e32 v136, 16, v137
	v_and_b32_e32 v137, 0xffff0000, v137
	v_pk_mul_f32 v[136:137], v[204:205], v[136:137] op_sel_hi:[0,1]
	v_pk_fma_f32 v[212:213], v[12:13], v[212:213], v[44:45]
	v_pk_fma_f32 v[136:137], v[14:15], v[136:137], v[46:47]
	v_cvt_pk_fp8_f32 v215, v212, v213
	v_cvt_pk_fp8_f32 v215, v136, v137 op_sel:[0,0,1]
	global_store_dword v[210:211], v215, off offset:768 sc0 sc1
	v_lshlrev_b32_e32 v212, 16, v138
	v_and_b32_e32 v213, 0xffff0000, v138
	v_pk_mul_f32 v[212:213], v[204:205], v[212:213] op_sel_hi:[0,1]
	v_lshlrev_b32_e32 v138, 16, v139
	v_and_b32_e32 v139, 0xffff0000, v139
	v_pk_mul_f32 v[138:139], v[204:205], v[138:139] op_sel_hi:[0,1]
	v_pk_fma_f32 v[212:213], v[16:17], v[212:213], v[48:49]
	v_pk_fma_f32 v[138:139], v[18:19], v[138:139], v[50:51]
	v_cvt_pk_fp8_f32 v214, v212, v213
	v_cvt_pk_fp8_f32 v214, v138, v139 op_sel:[0,0,1]
	global_store_dword v[210:211], v214, off offset:1024 sc0 sc1
	v_lshlrev_b32_e32 v212, 16, v140
	v_and_b32_e32 v213, 0xffff0000, v140
	v_pk_mul_f32 v[212:213], v[204:205], v[212:213] op_sel_hi:[0,1]
	v_lshlrev_b32_e32 v140, 16, v141
	v_and_b32_e32 v141, 0xffff0000, v141
	v_pk_mul_f32 v[140:141], v[204:205], v[140:141] op_sel_hi:[0,1]
	v_pk_fma_f32 v[212:213], v[20:21], v[212:213], v[52:53]
	v_pk_fma_f32 v[140:141], v[22:23], v[140:141], v[54:55]
	v_cvt_pk_fp8_f32 v215, v212, v213
	v_cvt_pk_fp8_f32 v215, v140, v141 op_sel:[0,0,1]
	global_store_dword v[210:211], v215, off offset:1280 sc0 sc1
	v_lshlrev_b32_e32 v212, 16, v142
	v_and_b32_e32 v213, 0xffff0000, v142
	v_pk_mul_f32 v[212:213], v[204:205], v[212:213] op_sel_hi:[0,1]
	v_lshlrev_b32_e32 v142, 16, v143
	v_and_b32_e32 v143, 0xffff0000, v143
	v_pk_mul_f32 v[142:143], v[204:205], v[142:143] op_sel_hi:[0,1]
	v_pk_fma_f32 v[212:213], v[24:25], v[212:213], v[56:57]
	v_pk_fma_f32 v[142:143], v[26:27], v[142:143], v[58:59]
	v_cvt_pk_fp8_f32 v214, v212, v213
	v_cvt_pk_fp8_f32 v214, v142, v143 op_sel:[0,0,1]
	global_store_dword v[210:211], v214, off offset:1536 sc0 sc1
	v_lshlrev_b32_e32 v212, 16, v144
	v_and_b32_e32 v213, 0xffff0000, v144
	v_pk_mul_f32 v[212:213], v[204:205], v[212:213] op_sel_hi:[0,1]
	v_lshlrev_b32_e32 v144, 16, v145
	v_and_b32_e32 v145, 0xffff0000, v145
	v_pk_mul_f32 v[144:145], v[204:205], v[144:145] op_sel_hi:[0,1]
	v_pk_fma_f32 v[212:213], v[28:29], v[212:213], v[198:199]
	v_pk_fma_f32 v[144:145], v[30:31], v[144:145], v[200:201]
	v_cvt_pk_fp8_f32 v215, v212, v213
	v_cvt_pk_fp8_f32 v215, v144, v145 op_sel:[0,0,1]
	global_store_dword v[210:211], v215, off offset:1792 sc0 sc1
	s_add_u32 s4, s4, 0x800
	v_lshl_add_u64 v[210:211], v[68:69], 0, s[4:5]
	s_waitcnt vmcnt(24)
; __device__ __forceinline__ void phase_router(const Args& a, unsigned char* lds_g, int tid, int lane, int wave) {
;     ...
;         for (int r = 0; r < 4; ++r) { const int tl = 4 * kq + r, t = tok0 + tl; const float rstd = RS[slot * 16 + tl];
;             const unsigned long long* xrow = (const unsigned long long*)(X1 + (size_t)t * D) + lane; unsigned* o4 = (unsigned*)((unsigned char*)H2 + (size_t)t * D) + lane;
;             f32x4 yv[8];
; #pragma unroll
;             for (int j = 0; j < 8; ++j) { const int c = 4 * lane + 256 * j;
;                 f32x4 gs, sh; if (shp) { gs = PSH[lane + 64 * j]; sh = PSH[512 + lane + 64 * j]; } else { const f32x4 gg = *(const f32x4*)(g + c), sc = *(const f32x4*)(MOD + b * 12288 + 4 * 2048 + c); gs = gg * (sc + 1.f); sh = *(const f32x4*)(MOD + b * 12288 + 3 * 2048 + c); }
;                 const unsigned long long xw = xrow[64 * j]; const f32x4 xv4 = (f32x4){bflo((unsigned)xw), bfhi((unsigned)xw), bflo((unsigned)(xw >> 32)), bfhi((unsigned)(xw >> 32))};
;                 yv[j] = xv4 * rstd * gs + sh; }
; #pragma unroll
;             for (int j = 0; j < 8; ++j) { int w8 = __builtin_amdgcn_cvt_pk_fp8_f32(yv[j].x, yv[j].y, 0, false); w8 = __builtin_amdgcn_cvt_pk_fp8_f32(yv[j].z, yv[j].w, w8, true); o4[64 * j] = (unsigned)w8; } }
	v_lshlrev_b32_e32 v212, 16, v146
	v_and_b32_e32 v213, 0xffff0000, v146
	v_pk_mul_f32 v[212:213], v[206:207], v[212:213] op_sel_hi:[0,1]
	v_lshlrev_b32_e32 v146, 16, v147
	v_and_b32_e32 v147, 0xffff0000, v147
	v_pk_mul_f32 v[146:147], v[206:207], v[146:147] op_sel_hi:[0,1]
	v_pk_fma_f32 v[212:213], v[0:1], v[212:213], v[32:33]
	v_pk_fma_f32 v[146:147], v[2:3], v[146:147], v[34:35]
	v_cvt_pk_fp8_f32 v214, v212, v213
	v_cvt_pk_fp8_f32 v214, v146, v147 op_sel:[0,0,1]
	global_store_dword v[210:211], v214, off sc0 sc1
	v_lshlrev_b32_e32 v212, 16, v148
	v_and_b32_e32 v213, 0xffff0000, v148
	v_pk_mul_f32 v[212:213], v[206:207], v[212:213] op_sel_hi:[0,1]
	v_lshlrev_b32_e32 v148, 16, v149
	v_and_b32_e32 v149, 0xffff0000, v149
	v_pk_mul_f32 v[148:149], v[206:207], v[148:149] op_sel_hi:[0,1]
	v_pk_fma_f32 v[212:213], v[4:5], v[212:213], v[36:37]
	v_pk_fma_f32 v[148:149], v[6:7], v[148:149], v[38:39]
	v_cvt_pk_fp8_f32 v215, v212, v213
	v_cvt_pk_fp8_f32 v215, v148, v149 op_sel:[0,0,1]
	global_store_dword v[210:211], v215, off offset:256 sc0 sc1
	v_lshlrev_b32_e32 v212, 16, v150
	v_and_b32_e32 v213, 0xffff0000, v150
	v_pk_mul_f32 v[212:213], v[206:207], v[212:213] op_sel_hi:[0,1]
	v_lshlrev_b32_e32 v150, 16, v151
	v_and_b32_e32 v151, 0xffff0000, v151
	v_pk_mul_f32 v[150:151], v[206:207], v[150:151] op_sel_hi:[0,1]
	v_pk_fma_f32 v[212:213], v[8:9], v[212:213], v[40:41]
	v_pk_fma_f32 v[150:151], v[10:11], v[150:151], v[42:43]
	v_cvt_pk_fp8_f32 v214, v212, v213
	v_cvt_pk_fp8_f32 v214, v150, v151 op_sel:[0,0,1]
	global_store_dword v[210:211], v214, off offset:512 sc0 sc1
	v_lshlrev_b32_e32 v212, 16, v152
	v_and_b32_e32 v213, 0xffff0000, v152
	v_pk_mul_f32 v[212:213], v[206:207], v[212:213] op_sel_hi:[0,1]
	v_lshlrev_b32_e32 v152, 16, v153
	v_and_b32_e32 v153, 0xffff0000, v153
	v_pk_mul_f32 v[152:153], v[206:207], v[152:153] op_sel_hi:[0,1]
	v_pk_fma_f32 v[212:213], v[12:13], v[212:213], v[44:45]
	v_pk_fma_f32 v[152:153], v[14:15], v[152:153], v[46:47]
	v_cvt_pk_fp8_f32 v215, v212, v213
	v_cvt_pk_fp8_f32 v215, v152, v153 op_sel:[0,0,1]
	global_store_dword v[210:211], v215, off offset:768 sc0 sc1
	v_lshlrev_b32_e32 v212, 16, v154
	v_and_b32_e32 v213, 0xffff0000, v154
	v_pk_mul_f32 v[212:213], v[206:207], v[212:213] op_sel_hi:[0,1]
	v_lshlrev_b32_e32 v154, 16, v155
	v_and_b32_e32 v155, 0xffff0000, v155
	v_pk_mul_f32 v[154:155], v[206:207], v[154:155] op_sel_hi:[0,1]
	v_pk_fma_f32 v[212:213], v[16:17], v[212:213], v[48:49]
	v_pk_fma_f32 v[154:155], v[18:19], v[154:155], v[50:51]
	v_cvt_pk_fp8_f32 v214, v212, v213
	v_cvt_pk_fp8_f32 v214, v154, v155 op_sel:[0,0,1]
	global_store_dword v[210:211], v214, off offset:1024 sc0 sc1
	v_lshlrev_b32_e32 v212, 16, v156
	v_and_b32_e32 v213, 0xffff0000, v156
	v_pk_mul_f32 v[212:213], v[206:207], v[212:213] op_sel_hi:[0,1]
	v_lshlrev_b32_e32 v156, 16, v157
	v_and_b32_e32 v157, 0xffff0000, v157
	v_pk_mul_f32 v[156:157], v[206:207], v[156:157] op_sel_hi:[0,1]
	v_pk_fma_f32 v[212:213], v[20:21], v[212:213], v[52:53]
	v_pk_fma_f32 v[156:157], v[22:23], v[156:157], v[54:55]
	v_cvt_pk_fp8_f32 v215, v212, v213
	v_cvt_pk_fp8_f32 v215, v156, v157 op_sel:[0,0,1]
	global_store_dword v[210:211], v215, off offset:1280 sc0 sc1
	v_lshlrev_b32_e32 v212, 16, v158
	v_and_b32_e32 v213, 0xffff0000, v158
	v_pk_mul_f32 v[212:213], v[206:207], v[212:213] op_sel_hi:[0,1]
	v_lshlrev_b32_e32 v158, 16, v159
	v_and_b32_e32 v159, 0xffff0000, v159
	v_pk_mul_f32 v[158:159], v[206:207], v[158:159] op_sel_hi:[0,1]
	v_pk_fma_f32 v[212:213], v[24:25], v[212:213], v[56:57]
	v_pk_fma_f32 v[158:159], v[26:27], v[158:159], v[58:59]
	v_cvt_pk_fp8_f32 v214, v212, v213
	v_cvt_pk_fp8_f32 v214, v158, v159 op_sel:[0,0,1]
	global_store_dword v[210:211], v214, off offset:1536 sc0 sc1
	v_lshlrev_b32_e32 v212, 16, v160
	v_and_b32_e32 v213, 0xffff0000, v160
	v_pk_mul_f32 v[212:213], v[206:207], v[212:213] op_sel_hi:[0,1]
	v_lshlrev_b32_e32 v160, 16, v161
	v_and_b32_e32 v161, 0xffff0000, v161
	v_pk_mul_f32 v[160:161], v[206:207], v[160:161] op_sel_hi:[0,1]
	v_pk_fma_f32 v[212:213], v[28:29], v[212:213], v[198:199]
	v_pk_fma_f32 v[160:161], v[30:31], v[160:161], v[200:201]
	v_cvt_pk_fp8_f32 v215, v212, v213
	v_cvt_pk_fp8_f32 v215, v160, v161 op_sel:[0,0,1]
	global_store_dword v[210:211], v215, off offset:1792 sc0 sc1
	s_add_u32 s4, s4, 0x800
	v_lshl_add_u64 v[210:211], v[68:69], 0, s[4:5]
	s_waitcnt vmcnt(24)
; __device__ __forceinline__ void phase_router(const Args& a, unsigned char* lds_g, int tid, int lane, int wave) {
;     ...
;         for (int r = 0; r < 4; ++r) { const int tl = 4 * kq + r, t = tok0 + tl; const float rstd = RS[slot * 16 + tl];
;             const unsigned long long* xrow = (const unsigned long long*)(X1 + (size_t)t * D) + lane; unsigned* o4 = (unsigned*)((unsigned char*)H2 + (size_t)t * D) + lane;
;             f32x4 yv[8];
; #pragma unroll
;             for (int j = 0; j < 8; ++j) { const int c = 4 * lane + 256 * j;
;                 f32x4 gs, sh; if (shp) { gs = PSH[lane + 64 * j]; sh = PSH[512 + lane + 64 * j]; } else { const f32x4 gg = *(const f32x4*)(g + c), sc = *(const f32x4*)(MOD + b * 12288 + 4 * 2048 + c); gs = gg * (sc + 1.f); sh = *(const f32x4*)(MOD + b * 12288 + 3 * 2048 + c); }
;                 const unsigned long long xw = xrow[64 * j]; const f32x4 xv4 = (f32x4){bflo((unsigned)xw), bfhi((unsigned)xw), bflo((unsigned)(xw >> 32)), bfhi((unsigned)(xw >> 32))};
;                 yv[j] = xv4 * rstd * gs + sh; }
; #pragma unroll
;             for (int j = 0; j < 8; ++j) { int w8 = __builtin_amdgcn_cvt_pk_fp8_f32(yv[j].x, yv[j].y, 0, false); w8 = __builtin_amdgcn_cvt_pk_fp8_f32(yv[j].z, yv[j].w, w8, true); o4[64 * j] = (unsigned)w8; } }
;         __syncthreads();
;     }
	v_lshlrev_b32_e32 v212, 16, v162
	v_and_b32_e32 v213, 0xffff0000, v162
	v_pk_mul_f32 v[212:213], v[208:209], v[212:213] op_sel_hi:[0,1]
	v_lshlrev_b32_e32 v162, 16, v163
	v_and_b32_e32 v163, 0xffff0000, v163
	v_pk_mul_f32 v[162:163], v[208:209], v[162:163] op_sel_hi:[0,1]
	v_pk_fma_f32 v[212:213], v[0:1], v[212:213], v[32:33]
	v_pk_fma_f32 v[162:163], v[2:3], v[162:163], v[34:35]
	v_cvt_pk_fp8_f32 v214, v212, v213
	v_cvt_pk_fp8_f32 v214, v162, v163 op_sel:[0,0,1]
	global_store_dword v[210:211], v214, off sc0 sc1
	v_lshlrev_b32_e32 v212, 16, v164
	v_and_b32_e32 v213, 0xffff0000, v164
	v_pk_mul_f32 v[212:213], v[208:209], v[212:213] op_sel_hi:[0,1]
	v_lshlrev_b32_e32 v164, 16, v165
	v_and_b32_e32 v165, 0xffff0000, v165
	v_pk_mul_f32 v[164:165], v[208:209], v[164:165] op_sel_hi:[0,1]
	v_pk_fma_f32 v[212:213], v[4:5], v[212:213], v[36:37]
	v_pk_fma_f32 v[164:165], v[6:7], v[164:165], v[38:39]
	v_cvt_pk_fp8_f32 v215, v212, v213
	v_cvt_pk_fp8_f32 v215, v164, v165 op_sel:[0,0,1]
	global_store_dword v[210:211], v215, off offset:256 sc0 sc1
	v_lshlrev_b32_e32 v212, 16, v166
	v_and_b32_e32 v213, 0xffff0000, v166
	v_pk_mul_f32 v[212:213], v[208:209], v[212:213] op_sel_hi:[0,1]
	v_lshlrev_b32_e32 v166, 16, v167
	v_and_b32_e32 v167, 0xffff0000, v167
	v_pk_mul_f32 v[166:167], v[208:209], v[166:167] op_sel_hi:[0,1]
	v_pk_fma_f32 v[212:213], v[8:9], v[212:213], v[40:41]
	v_pk_fma_f32 v[166:167], v[10:11], v[166:167], v[42:43]
	v_cvt_pk_fp8_f32 v214, v212, v213
	v_cvt_pk_fp8_f32 v214, v166, v167 op_sel:[0,0,1]
	global_store_dword v[210:211], v214, off offset:512 sc0 sc1
	v_lshlrev_b32_e32 v212, 16, v168
	v_and_b32_e32 v213, 0xffff0000, v168
	v_pk_mul_f32 v[212:213], v[208:209], v[212:213] op_sel_hi:[0,1]
	v_lshlrev_b32_e32 v168, 16, v169
	v_and_b32_e32 v169, 0xffff0000, v169
	v_pk_mul_f32 v[168:169], v[208:209], v[168:169] op_sel_hi:[0,1]
	v_pk_fma_f32 v[212:213], v[12:13], v[212:213], v[44:45]
	v_pk_fma_f32 v[168:169], v[14:15], v[168:169], v[46:47]
	v_cvt_pk_fp8_f32 v215, v212, v213
	v_cvt_pk_fp8_f32 v215, v168, v169 op_sel:[0,0,1]
	global_store_dword v[210:211], v215, off offset:768 sc0 sc1
	v_lshlrev_b32_e32 v212, 16, v170
	v_and_b32_e32 v213, 0xffff0000, v170
	v_pk_mul_f32 v[212:213], v[208:209], v[212:213] op_sel_hi:[0,1]
	v_lshlrev_b32_e32 v170, 16, v171
	v_and_b32_e32 v171, 0xffff0000, v171
	v_pk_mul_f32 v[170:171], v[208:209], v[170:171] op_sel_hi:[0,1]
	v_pk_fma_f32 v[212:213], v[16:17], v[212:213], v[48:49]
	v_pk_fma_f32 v[170:171], v[18:19], v[170:171], v[50:51]
	v_cvt_pk_fp8_f32 v214, v212, v213
	v_cvt_pk_fp8_f32 v214, v170, v171 op_sel:[0,0,1]
	global_store_dword v[210:211], v214, off offset:1024 sc0 sc1
	v_lshlrev_b32_e32 v212, 16, v172
	v_and_b32_e32 v213, 0xffff0000, v172
	v_pk_mul_f32 v[212:213], v[208:209], v[212:213] op_sel_hi:[0,1]
	v_lshlrev_b32_e32 v172, 16, v173
	v_and_b32_e32 v173, 0xffff0000, v173
	v_pk_mul_f32 v[172:173], v[208:209], v[172:173] op_sel_hi:[0,1]
	v_pk_fma_f32 v[212:213], v[20:21], v[212:213], v[52:53]
	v_pk_fma_f32 v[172:173], v[22:23], v[172:173], v[54:55]
	v_cvt_pk_fp8_f32 v215, v212, v213
	v_cvt_pk_fp8_f32 v215, v172, v173 op_sel:[0,0,1]
	global_store_dword v[210:211], v215, off offset:1280 sc0 sc1
	v_lshlrev_b32_e32 v212, 16, v194
	v_and_b32_e32 v213, 0xffff0000, v194
	v_pk_mul_f32 v[212:213], v[208:209], v[212:213] op_sel_hi:[0,1]
	v_lshlrev_b32_e32 v194, 16, v195
	v_and_b32_e32 v195, 0xffff0000, v195
	v_pk_mul_f32 v[194:195], v[208:209], v[194:195] op_sel_hi:[0,1]
	v_pk_fma_f32 v[212:213], v[24:25], v[212:213], v[56:57]
	v_pk_fma_f32 v[194:195], v[26:27], v[194:195], v[58:59]
	v_cvt_pk_fp8_f32 v214, v212, v213
	v_cvt_pk_fp8_f32 v214, v194, v195 op_sel:[0,0,1]
	global_store_dword v[210:211], v214, off offset:1536 sc0 sc1
	v_lshlrev_b32_e32 v212, 16, v196
	v_and_b32_e32 v213, 0xffff0000, v196
	v_pk_mul_f32 v[212:213], v[208:209], v[212:213] op_sel_hi:[0,1]
	v_lshlrev_b32_e32 v196, 16, v197
	v_and_b32_e32 v197, 0xffff0000, v197
	v_pk_mul_f32 v[196:197], v[208:209], v[196:197] op_sel_hi:[0,1]
	v_pk_fma_f32 v[212:213], v[28:29], v[212:213], v[198:199]
	v_pk_fma_f32 v[196:197], v[30:31], v[196:197], v[200:201]
	v_cvt_pk_fp8_f32 v215, v212, v213
	v_cvt_pk_fp8_f32 v215, v196, v197 op_sel:[0,0,1]
	global_store_dword v[210:211], v215, off offset:1792 sc0 sc1
	s_add_i32 s55, s55, s82
	v_add_u32_e32 v106, s44, v106
	s_cmpk_lt_i32 s55, 0x100
	s_barrier
	s_cbranch_scc0 .LBB0_1113
	s_branch .LBB0_975
